# v28 + grid barrier: non-leader workgroups issue the agent-scope L1 invalidate on arrival (before polling) instead of after release
# baseline (speedup 1.0000x reference)
; __device__ __forceinline__ unsigned xb_ld(unsigned* p)              { return __hip_atomic_load(p, __ATOMIC_RELAXED, __HIP_MEMORY_SCOPE_AGENT); }
; __device__ __forceinline__ unsigned xb_add(unsigned* p, unsigned v) { return __hip_atomic_fetch_add(p, v, __ATOMIC_RELAXED, __HIP_MEMORY_SCOPE_AGENT); }
; #define XB_SPIN(cond, bar) do { unsigned _sp = 0; while (cond) { __builtin_amdgcn_s_sleep(1); \
;     if ((++_sp & 255u) == 0u) { if (xb_ld(&(bar)[XB_TMO])) break; if (_sp > XB_SPIN_CAP) { atomicAdd(&(bar)[XB_TMO], 1u); break; } } } } while (0)
; __device__ __forceinline__ void xcd_barrier(const XcdBarrier& b) {
;     ...
;         const unsigned old = xb_add(&bar[XB_XSUB(b.x)], 1u);
;         const unsigned gen = old / nloc;
;         if (old + 1u == (gen + 1u) * nloc) {
;             __builtin_amdgcn_fence(__ATOMIC_RELEASE, "agent");
;             asm volatile("s_waitcnt vmcnt(0)" ::: "memory");
;             const unsigned og = xb_add(&bar[XB_TOP], 1u);
;             const unsigned tg = og / nx;
;             if (og + 1u == (tg + 1u) * nx) xb_add(&bar[XB_TOPGEN], 1u);
;             else XB_SPIN(xb_ld(&bar[XB_TOPGEN]) == tg, bar);
;             __builtin_amdgcn_fence(__ATOMIC_ACQUIRE, "agent");
;             xb_add(&bar[XB_XGEN(b.x)], 1u);
;             asm volatile("s_waitcnt vmcnt(0)" ::: "memory");
;         } else {
;             XB_SPIN(xb_ld(&bar[XB_XGEN(b.x)]) == gen, bar);
;             __builtin_amdgcn_fence(__ATOMIC_ACQUIRE, "agent");
;             asm volatile("s_waitcnt vmcnt(0)" ::: "memory");
.LBB0_66:
	s_or_b64 exec, exec, s[12:13]
	v_cvt_f32_u32_e32 v5, v3
	s_waitcnt vmcnt(0)
	v_readfirstlane_b32 s10, v4
	v_sub_u32_e32 v4, 0, v3
	v_rcp_iflag_f32_e32 v5, v5
	v_add_u32_e32 v6, s10, v2
	v_mul_f32_e32 v5, 0x4f7ffffe, v5
	v_cvt_u32_f32_e32 v5, v5
	v_mul_lo_u32 v2, v4, v5
	v_mul_hi_u32 v2, v5, v2
	v_add_u32_e32 v2, v5, v2
	v_mul_hi_u32 v2, v6, v2
	v_mul_lo_u32 v4, v2, v3
	v_sub_u32_e32 v4, v6, v4
	v_add_u32_e32 v5, 1, v2
	v_cmp_ge_u32_e32 vcc, v4, v3
	s_nop 1
	v_cndmask_b32_e32 v2, v2, v5, vcc
	v_sub_u32_e32 v5, v4, v3
	v_cndmask_b32_e32 v4, v4, v5, vcc
	v_add_u32_e32 v5, 1, v2
	v_cmp_ge_u32_e32 vcc, v4, v3
	v_add_u32_e32 v4, 1, v6
	s_nop 0
	v_cndmask_b32_e32 v2, v2, v5, vcc
	v_mul_lo_u32 v5, v3, v2
	v_add_u32_e32 v3, v5, v3
	v_cmp_ne_u32_e32 vcc, v4, v3
	s_and_saveexec_b64 s[10:11], vcc
	s_xor_b64 s[10:11], exec, s[10:11]
	s_cbranch_execz .LBB0_80
	s_waitcnt lgkmcnt(0)
	buffer_inv sc1
	v_mov_b32_e32 v1, 0x2000
	global_load_dword v1, v1, s[8:9] offset:1024 sc1
	s_add_u32 s16, s8, 0x2400
	s_addc_u32 s17, s9, 0
	s_waitcnt vmcnt(0)
	v_cmp_eq_u32_e32 vcc, v1, v2
	s_and_saveexec_b64 s[12:13], vcc
	s_cbranch_execz .LBB0_79
	s_add_u32 s14, s30, 0x4200
	s_addc_u32 s15, s31, 0
	s_mov_b32 s27, 1
	s_mov_b64 s[18:19], 0
	v_mov_b32_e32 v1, 0
	s_branch .LBB0_70

; __device__ __forceinline__ unsigned xb_ld(unsigned* p)              { return __hip_atomic_load(p, __ATOMIC_RELAXED, __HIP_MEMORY_SCOPE_AGENT); }
; #define XB_SPIN(cond, bar) do { unsigned _sp = 0; while (cond) { __builtin_amdgcn_s_sleep(1); \
;     if ((++_sp & 255u) == 0u) { if (xb_ld(&(bar)[XB_TMO])) break; if (_sp > XB_SPIN_CAP) { atomicAdd(&(bar)[XB_TMO], 1u); break; } } } } while (0)
; __device__ __forceinline__ void xcd_barrier(const XcdBarrier& b) {
;     ...
;         } else {
;             XB_SPIN(xb_ld(&bar[XB_XGEN(b.x)]) == gen, bar);
;             __builtin_amdgcn_fence(__ATOMIC_ACQUIRE, "agent");
;             asm volatile("s_waitcnt vmcnt(0)" ::: "memory");
;         }
.LBB0_79:
	s_or_b64 exec, exec, s[12:13]
	s_waitcnt vmcnt(0)
	s_waitcnt vmcnt(0)

; __device__ __forceinline__ unsigned xb_ld(unsigned* p)              { return __hip_atomic_load(p, __ATOMIC_RELAXED, __HIP_MEMORY_SCOPE_AGENT); }
; __device__ __forceinline__ unsigned xb_add(unsigned* p, unsigned v) { return __hip_atomic_fetch_add(p, v, __ATOMIC_RELAXED, __HIP_MEMORY_SCOPE_AGENT); }
; #define XB_SPIN(cond, bar) do { unsigned _sp = 0; while (cond) { __builtin_amdgcn_s_sleep(1); \
;     if ((++_sp & 255u) == 0u) { if (xb_ld(&(bar)[XB_TMO])) break; if (_sp > XB_SPIN_CAP) { atomicAdd(&(bar)[XB_TMO], 1u); break; } } } } while (0)
; __device__ __forceinline__ void xcd_barrier(const XcdBarrier& b) {
;     ...
;         const unsigned old = xb_add(&bar[XB_XSUB(b.x)], 1u);
;         const unsigned gen = old / nloc;
;         if (old + 1u == (gen + 1u) * nloc) {
;             __builtin_amdgcn_fence(__ATOMIC_RELEASE, "agent");
;             asm volatile("s_waitcnt vmcnt(0)" ::: "memory");
;             const unsigned og = xb_add(&bar[XB_TOP], 1u);
;             const unsigned tg = og / nx;
;             if (og + 1u == (tg + 1u) * nx) xb_add(&bar[XB_TOPGEN], 1u);
;             else XB_SPIN(xb_ld(&bar[XB_TOPGEN]) == tg, bar);
;             __builtin_amdgcn_fence(__ATOMIC_ACQUIRE, "agent");
;             xb_add(&bar[XB_XGEN(b.x)], 1u);
;             asm volatile("s_waitcnt vmcnt(0)" ::: "memory");
;         } else {
;             XB_SPIN(xb_ld(&bar[XB_XGEN(b.x)]) == gen, bar);
;             __builtin_amdgcn_fence(__ATOMIC_ACQUIRE, "agent");
;             asm volatile("s_waitcnt vmcnt(0)" ::: "memory");
.LBB0_163:
	s_or_b64 exec, exec, s[12:13]
	v_cvt_f32_u32_e32 v5, v3
	s_waitcnt vmcnt(0)
	v_readfirstlane_b32 s10, v4
	v_sub_u32_e32 v4, 0, v3
	v_rcp_iflag_f32_e32 v5, v5
	v_add_u32_e32 v6, s10, v2
	v_mul_f32_e32 v5, 0x4f7ffffe, v5
	v_cvt_u32_f32_e32 v5, v5
	v_mul_lo_u32 v2, v4, v5
	v_mul_hi_u32 v2, v5, v2
	v_add_u32_e32 v2, v5, v2
	v_mul_hi_u32 v2, v6, v2
	v_mul_lo_u32 v4, v2, v3
	v_sub_u32_e32 v4, v6, v4
	v_add_u32_e32 v5, 1, v2
	v_cmp_ge_u32_e32 vcc, v4, v3
	s_nop 1
	v_cndmask_b32_e32 v2, v2, v5, vcc
	v_sub_u32_e32 v5, v4, v3
	v_cndmask_b32_e32 v4, v4, v5, vcc
	v_add_u32_e32 v5, 1, v2
	v_cmp_ge_u32_e32 vcc, v4, v3
	v_add_u32_e32 v4, 1, v6
	s_nop 0
	v_cndmask_b32_e32 v2, v2, v5, vcc
	v_mul_lo_u32 v5, v3, v2
	v_add_u32_e32 v3, v5, v3
	v_cmp_ne_u32_e32 vcc, v4, v3
	s_and_saveexec_b64 s[10:11], vcc
	s_xor_b64 s[10:11], exec, s[10:11]
	s_cbranch_execz .LBB0_177
	s_waitcnt lgkmcnt(0)
	v_mov_b32_e32 v1, 0x2000
	buffer_inv sc1
	global_load_dword v1, v1, s[8:9] offset:1024 sc1
	s_add_u32 s16, s8, 0x2400
	s_addc_u32 s17, s9, 0
	s_waitcnt vmcnt(0)
	v_cmp_eq_u32_e32 vcc, v1, v2
	s_and_saveexec_b64 s[12:13], vcc
	s_cbranch_execz .LBB0_176
	s_add_u32 s14, s30, 0x4200
	s_addc_u32 s15, s31, 0
	s_mov_b32 s27, 1
	s_mov_b64 s[18:19], 0
	v_mov_b32_e32 v1, 0
	s_branch .LBB0_167

; __device__ __forceinline__ unsigned xb_ld(unsigned* p)              { return __hip_atomic_load(p, __ATOMIC_RELAXED, __HIP_MEMORY_SCOPE_AGENT); }
; __device__ __forceinline__ unsigned xb_add(unsigned* p, unsigned v) { return __hip_atomic_fetch_add(p, v, __ATOMIC_RELAXED, __HIP_MEMORY_SCOPE_AGENT); }
; #define XB_SPIN(cond, bar) do { unsigned _sp = 0; while (cond) { __builtin_amdgcn_s_sleep(1); \
;     if ((++_sp & 255u) == 0u) { if (xb_ld(&(bar)[XB_TMO])) break; if (_sp > XB_SPIN_CAP) { atomicAdd(&(bar)[XB_TMO], 1u); break; } } } } while (0)
; __device__ __forceinline__ void xcd_barrier(const XcdBarrier& b) {
;     ...
;         const unsigned old = xb_add(&bar[XB_XSUB(b.x)], 1u);
;         const unsigned gen = old / nloc;
;         if (old + 1u == (gen + 1u) * nloc) {
;             __builtin_amdgcn_fence(__ATOMIC_RELEASE, "agent");
;             asm volatile("s_waitcnt vmcnt(0)" ::: "memory");
;             const unsigned og = xb_add(&bar[XB_TOP], 1u);
;             const unsigned tg = og / nx;
;             if (og + 1u == (tg + 1u) * nx) xb_add(&bar[XB_TOPGEN], 1u);
;             else XB_SPIN(xb_ld(&bar[XB_TOPGEN]) == tg, bar);
;             __builtin_amdgcn_fence(__ATOMIC_ACQUIRE, "agent");
;             xb_add(&bar[XB_XGEN(b.x)], 1u);
;             asm volatile("s_waitcnt vmcnt(0)" ::: "memory");
;         } else {
;             XB_SPIN(xb_ld(&bar[XB_XGEN(b.x)]) == gen, bar);
;             __builtin_amdgcn_fence(__ATOMIC_ACQUIRE, "agent");
;             asm volatile("s_waitcnt vmcnt(0)" ::: "memory");
.LBB0_221:
	s_or_b64 exec, exec, s[12:13]
	v_cvt_f32_u32_e32 v5, v3
	s_waitcnt vmcnt(0)
	v_readfirstlane_b32 s10, v4
	v_sub_u32_e32 v4, 0, v3
	v_rcp_iflag_f32_e32 v5, v5
	v_add_u32_e32 v6, s10, v2
	v_mul_f32_e32 v5, 0x4f7ffffe, v5
	v_cvt_u32_f32_e32 v5, v5
	v_mul_lo_u32 v2, v4, v5
	v_mul_hi_u32 v2, v5, v2
	v_add_u32_e32 v2, v5, v2
	v_mul_hi_u32 v2, v6, v2
	v_mul_lo_u32 v4, v2, v3
	v_sub_u32_e32 v4, v6, v4
	v_add_u32_e32 v5, 1, v2
	v_cmp_ge_u32_e32 vcc, v4, v3
	s_nop 1
	v_cndmask_b32_e32 v2, v2, v5, vcc
	v_sub_u32_e32 v5, v4, v3
	v_cndmask_b32_e32 v4, v4, v5, vcc
	v_add_u32_e32 v5, 1, v2
	v_cmp_ge_u32_e32 vcc, v4, v3
	v_add_u32_e32 v4, 1, v6
	s_nop 0
	v_cndmask_b32_e32 v2, v2, v5, vcc
	v_mul_lo_u32 v5, v3, v2
	v_add_u32_e32 v3, v5, v3
	v_cmp_ne_u32_e32 vcc, v4, v3
	s_and_saveexec_b64 s[10:11], vcc
	s_xor_b64 s[10:11], exec, s[10:11]
	s_cbranch_execz .LBB0_235
	s_waitcnt lgkmcnt(0)
	v_mov_b32_e32 v1, 0x2000
	global_load_dword v1, v1, s[8:9] offset:1024 sc1
	buffer_inv sc1
	s_add_u32 s16, s8, 0x2400
	s_addc_u32 s17, s9, 0
	s_waitcnt vmcnt(0)
	v_cmp_eq_u32_e32 vcc, v1, v2
	s_and_saveexec_b64 s[12:13], vcc
	s_cbranch_execz .LBB0_234
	s_add_u32 s14, s30, 0x4200
	s_addc_u32 s15, s31, 0
	s_mov_b32 s27, 1
	s_mov_b64 s[18:19], 0
	v_mov_b32_e32 v1, 0
	s_branch .LBB0_225

; __device__ __forceinline__ unsigned xb_ld(unsigned* p)              { return __hip_atomic_load(p, __ATOMIC_RELAXED, __HIP_MEMORY_SCOPE_AGENT); }
; __device__ __forceinline__ unsigned xb_add(unsigned* p, unsigned v) { return __hip_atomic_fetch_add(p, v, __ATOMIC_RELAXED, __HIP_MEMORY_SCOPE_AGENT); }
; #define XB_SPIN(cond, bar) do { unsigned _sp = 0; while (cond) { __builtin_amdgcn_s_sleep(1); \
;     if ((++_sp & 255u) == 0u) { if (xb_ld(&(bar)[XB_TMO])) break; if (_sp > XB_SPIN_CAP) { atomicAdd(&(bar)[XB_TMO], 1u); break; } } } } while (0)
; __device__ __forceinline__ void xcd_barrier(const XcdBarrier& b) {
;     ...
;         const unsigned old = xb_add(&bar[XB_XSUB(b.x)], 1u);
;         const unsigned gen = old / nloc;
;         if (old + 1u == (gen + 1u) * nloc) {
;             __builtin_amdgcn_fence(__ATOMIC_RELEASE, "agent");
;             asm volatile("s_waitcnt vmcnt(0)" ::: "memory");
;             const unsigned og = xb_add(&bar[XB_TOP], 1u);
;             const unsigned tg = og / nx;
;             if (og + 1u == (tg + 1u) * nx) xb_add(&bar[XB_TOPGEN], 1u);
;             else XB_SPIN(xb_ld(&bar[XB_TOPGEN]) == tg, bar);
;             __builtin_amdgcn_fence(__ATOMIC_ACQUIRE, "agent");
;             xb_add(&bar[XB_XGEN(b.x)], 1u);
;             asm volatile("s_waitcnt vmcnt(0)" ::: "memory");
;         } else {
;             XB_SPIN(xb_ld(&bar[XB_XGEN(b.x)]) == gen, bar);
;             __builtin_amdgcn_fence(__ATOMIC_ACQUIRE, "agent");
;             asm volatile("s_waitcnt vmcnt(0)" ::: "memory");
.LBB0_301:
	s_or_b64 exec, exec, s[12:13]
	v_cvt_f32_u32_e32 v5, v3
	s_waitcnt vmcnt(0)
	v_readfirstlane_b32 s10, v4
	v_sub_u32_e32 v4, 0, v3
	v_rcp_iflag_f32_e32 v5, v5
	v_add_u32_e32 v6, s10, v2
	v_mul_f32_e32 v5, 0x4f7ffffe, v5
	v_cvt_u32_f32_e32 v5, v5
	v_mul_lo_u32 v2, v4, v5
	v_mul_hi_u32 v2, v5, v2
	v_add_u32_e32 v2, v5, v2
	v_mul_hi_u32 v2, v6, v2
	v_mul_lo_u32 v4, v2, v3
	v_sub_u32_e32 v4, v6, v4
	v_add_u32_e32 v5, 1, v2
	v_cmp_ge_u32_e32 vcc, v4, v3
	s_nop 1
	v_cndmask_b32_e32 v2, v2, v5, vcc
	v_sub_u32_e32 v5, v4, v3
	v_cndmask_b32_e32 v4, v4, v5, vcc
	v_add_u32_e32 v5, 1, v2
	v_cmp_ge_u32_e32 vcc, v4, v3
	v_add_u32_e32 v4, 1, v6
	s_nop 0
	v_cndmask_b32_e32 v2, v2, v5, vcc
	v_mul_lo_u32 v5, v3, v2
	v_add_u32_e32 v3, v5, v3
	v_cmp_ne_u32_e32 vcc, v4, v3
	s_and_saveexec_b64 s[10:11], vcc
	s_xor_b64 s[10:11], exec, s[10:11]
	s_cbranch_execz .LBB0_315
	s_waitcnt lgkmcnt(0)
	v_mov_b32_e32 v1, 0x2000
	global_load_dword v1, v1, s[8:9] offset:1024 sc1
	s_add_u32 s16, s8, 0x2400
	buffer_inv sc1
	s_addc_u32 s17, s9, 0
	s_waitcnt vmcnt(0)
	v_cmp_eq_u32_e32 vcc, v1, v2
	s_and_saveexec_b64 s[12:13], vcc
	s_cbranch_execz .LBB0_314
	s_add_u32 s14, s30, 0x4200
	s_addc_u32 s15, s31, 0
	s_mov_b32 s27, 1
	s_mov_b64 s[18:19], 0
	v_mov_b32_e32 v1, 0
	s_branch .LBB0_305

; __device__ __forceinline__ unsigned xb_ld(unsigned* p)              { return __hip_atomic_load(p, __ATOMIC_RELAXED, __HIP_MEMORY_SCOPE_AGENT); }
; __device__ __forceinline__ unsigned xb_add(unsigned* p, unsigned v) { return __hip_atomic_fetch_add(p, v, __ATOMIC_RELAXED, __HIP_MEMORY_SCOPE_AGENT); }
; #define XB_SPIN(cond, bar) do { unsigned _sp = 0; while (cond) { __builtin_amdgcn_s_sleep(1); \
;     if ((++_sp & 255u) == 0u) { if (xb_ld(&(bar)[XB_TMO])) break; if (_sp > XB_SPIN_CAP) { atomicAdd(&(bar)[XB_TMO], 1u); break; } } } } while (0)
; __device__ __forceinline__ void xcd_barrier(const XcdBarrier& b) {
;     ...
;         const unsigned old = xb_add(&bar[XB_XSUB(b.x)], 1u);
;         const unsigned gen = old / nloc;
;         if (old + 1u == (gen + 1u) * nloc) {
;             __builtin_amdgcn_fence(__ATOMIC_RELEASE, "agent");
;             asm volatile("s_waitcnt vmcnt(0)" ::: "memory");
;             const unsigned og = xb_add(&bar[XB_TOP], 1u);
;             const unsigned tg = og / nx;
;             if (og + 1u == (tg + 1u) * nx) xb_add(&bar[XB_TOPGEN], 1u);
;             else XB_SPIN(xb_ld(&bar[XB_TOPGEN]) == tg, bar);
;             __builtin_amdgcn_fence(__ATOMIC_ACQUIRE, "agent");
;             xb_add(&bar[XB_XGEN(b.x)], 1u);
;             asm volatile("s_waitcnt vmcnt(0)" ::: "memory");
;         } else {
;             XB_SPIN(xb_ld(&bar[XB_XGEN(b.x)]) == gen, bar);
;             __builtin_amdgcn_fence(__ATOMIC_ACQUIRE, "agent");
;             asm volatile("s_waitcnt vmcnt(0)" ::: "memory");
.LBB0_371:
	s_or_b64 exec, exec, s[12:13]
	v_cvt_f32_u32_e32 v5, v3
	s_waitcnt vmcnt(0)
	v_readfirstlane_b32 s10, v4
	v_sub_u32_e32 v4, 0, v3
	v_rcp_iflag_f32_e32 v5, v5
	v_add_u32_e32 v6, s10, v2
	v_mul_f32_e32 v5, 0x4f7ffffe, v5
	v_cvt_u32_f32_e32 v5, v5
	v_mul_lo_u32 v2, v4, v5
	v_mul_hi_u32 v2, v5, v2
	v_add_u32_e32 v2, v5, v2
	v_mul_hi_u32 v2, v6, v2
	v_mul_lo_u32 v4, v2, v3
	v_sub_u32_e32 v4, v6, v4
	v_add_u32_e32 v5, 1, v2
	v_cmp_ge_u32_e32 vcc, v4, v3
	s_nop 1
	v_cndmask_b32_e32 v2, v2, v5, vcc
	v_sub_u32_e32 v5, v4, v3
	v_cndmask_b32_e32 v4, v4, v5, vcc
	v_add_u32_e32 v5, 1, v2
	v_cmp_ge_u32_e32 vcc, v4, v3
	v_add_u32_e32 v4, 1, v6
	s_nop 0
	v_cndmask_b32_e32 v2, v2, v5, vcc
	v_mul_lo_u32 v5, v3, v2
	v_add_u32_e32 v3, v5, v3
	v_cmp_ne_u32_e32 vcc, v4, v3
	s_and_saveexec_b64 s[10:11], vcc
	s_xor_b64 s[10:11], exec, s[10:11]
	s_cbranch_execz .LBB0_385
	s_waitcnt lgkmcnt(0)
	v_mov_b32_e32 v1, 0x2000
	global_load_dword v1, v1, s[8:9] offset:1024 sc1
	s_add_u32 s16, s8, 0x2400
	s_addc_u32 s17, s9, 0
	buffer_inv sc1
	s_waitcnt vmcnt(0)
	v_cmp_eq_u32_e32 vcc, v1, v2
	s_and_saveexec_b64 s[12:13], vcc
	s_cbranch_execz .LBB0_384
	s_add_u32 s14, s30, 0x4200
	s_addc_u32 s15, s31, 0
	s_mov_b32 s27, 1
	s_mov_b64 s[18:19], 0
	v_mov_b32_e32 v1, 0
	s_branch .LBB0_375

; __device__ __forceinline__ unsigned xb_ld(unsigned* p)              { return __hip_atomic_load(p, __ATOMIC_RELAXED, __HIP_MEMORY_SCOPE_AGENT); }
; __device__ __forceinline__ unsigned xb_add(unsigned* p, unsigned v) { return __hip_atomic_fetch_add(p, v, __ATOMIC_RELAXED, __HIP_MEMORY_SCOPE_AGENT); }
; #define XB_SPIN(cond, bar) do { unsigned _sp = 0; while (cond) { __builtin_amdgcn_s_sleep(1); \
;     if ((++_sp & 255u) == 0u) { if (xb_ld(&(bar)[XB_TMO])) break; if (_sp > XB_SPIN_CAP) { atomicAdd(&(bar)[XB_TMO], 1u); break; } } } } while (0)
; __device__ __forceinline__ void xcd_barrier(const XcdBarrier& b) {
;     ...
;         const unsigned old = xb_add(&bar[XB_XSUB(b.x)], 1u);
;         const unsigned gen = old / nloc;
;         if (old + 1u == (gen + 1u) * nloc) {
;             __builtin_amdgcn_fence(__ATOMIC_RELEASE, "agent");
;             asm volatile("s_waitcnt vmcnt(0)" ::: "memory");
;             const unsigned og = xb_add(&bar[XB_TOP], 1u);
;             const unsigned tg = og / nx;
;             if (og + 1u == (tg + 1u) * nx) xb_add(&bar[XB_TOPGEN], 1u);
;             else XB_SPIN(xb_ld(&bar[XB_TOPGEN]) == tg, bar);
;             __builtin_amdgcn_fence(__ATOMIC_ACQUIRE, "agent");
;             xb_add(&bar[XB_XGEN(b.x)], 1u);
;             asm volatile("s_waitcnt vmcnt(0)" ::: "memory");
;         } else {
;             XB_SPIN(xb_ld(&bar[XB_XGEN(b.x)]) == gen, bar);
;             __builtin_amdgcn_fence(__ATOMIC_ACQUIRE, "agent");
;             asm volatile("s_waitcnt vmcnt(0)" ::: "memory");
.LBB0_469:
	s_or_b64 exec, exec, s[12:13]
	v_cvt_f32_u32_e32 v5, v3
	s_waitcnt vmcnt(0)
	v_readfirstlane_b32 s10, v4
	v_sub_u32_e32 v4, 0, v3
	v_rcp_iflag_f32_e32 v5, v5
	v_add_u32_e32 v6, s10, v2
	v_mul_f32_e32 v5, 0x4f7ffffe, v5
	v_cvt_u32_f32_e32 v5, v5
	v_mul_lo_u32 v2, v4, v5
	v_mul_hi_u32 v2, v5, v2
	v_add_u32_e32 v2, v5, v2
	v_mul_hi_u32 v2, v6, v2
	v_mul_lo_u32 v4, v2, v3
	v_sub_u32_e32 v4, v6, v4
	v_add_u32_e32 v5, 1, v2
	v_cmp_ge_u32_e32 vcc, v4, v3
	s_nop 1
	v_cndmask_b32_e32 v2, v2, v5, vcc
	v_sub_u32_e32 v5, v4, v3
	v_cndmask_b32_e32 v4, v4, v5, vcc
	v_add_u32_e32 v5, 1, v2
	v_cmp_ge_u32_e32 vcc, v4, v3
	v_add_u32_e32 v4, 1, v6
	s_nop 0
	v_cndmask_b32_e32 v2, v2, v5, vcc
	v_mul_lo_u32 v5, v3, v2
	v_add_u32_e32 v3, v5, v3
	v_cmp_ne_u32_e32 vcc, v4, v3
	s_and_saveexec_b64 s[10:11], vcc
	s_xor_b64 s[10:11], exec, s[10:11]
	s_cbranch_execz .LBB0_483
	s_waitcnt lgkmcnt(0)
	v_mov_b32_e32 v1, 0x2000
	global_load_dword v1, v1, s[8:9] offset:1024 sc1
	s_add_u32 s16, s8, 0x2400
	s_addc_u32 s17, s9, 0
	s_waitcnt vmcnt(0)
	buffer_inv sc1
	v_cmp_eq_u32_e32 vcc, v1, v2
	s_and_saveexec_b64 s[12:13], vcc
	s_cbranch_execz .LBB0_482
	s_add_u32 s14, s30, 0x4200
	s_addc_u32 s15, s31, 0
	s_mov_b32 s27, 1
	s_mov_b64 s[18:19], 0
	v_mov_b32_e32 v1, 0
	s_branch .LBB0_473

; __device__ __forceinline__ unsigned xb_ld(unsigned* p)              { return __hip_atomic_load(p, __ATOMIC_RELAXED, __HIP_MEMORY_SCOPE_AGENT); }
; __device__ __forceinline__ unsigned xb_add(unsigned* p, unsigned v) { return __hip_atomic_fetch_add(p, v, __ATOMIC_RELAXED, __HIP_MEMORY_SCOPE_AGENT); }
; #define XB_SPIN(cond, bar) do { unsigned _sp = 0; while (cond) { __builtin_amdgcn_s_sleep(1); \
;     if ((++_sp & 255u) == 0u) { if (xb_ld(&(bar)[XB_TMO])) break; if (_sp > XB_SPIN_CAP) { atomicAdd(&(bar)[XB_TMO], 1u); break; } } } } while (0)
; __device__ __forceinline__ void xcd_barrier(const XcdBarrier& b) {
;     ...
;         const unsigned old = xb_add(&bar[XB_XSUB(b.x)], 1u);
;         const unsigned gen = old / nloc;
;         if (old + 1u == (gen + 1u) * nloc) {
;             __builtin_amdgcn_fence(__ATOMIC_RELEASE, "agent");
;             asm volatile("s_waitcnt vmcnt(0)" ::: "memory");
;             const unsigned og = xb_add(&bar[XB_TOP], 1u);
;             const unsigned tg = og / nx;
;             if (og + 1u == (tg + 1u) * nx) xb_add(&bar[XB_TOPGEN], 1u);
;             else XB_SPIN(xb_ld(&bar[XB_TOPGEN]) == tg, bar);
;             __builtin_amdgcn_fence(__ATOMIC_ACQUIRE, "agent");
;             xb_add(&bar[XB_XGEN(b.x)], 1u);
;             asm volatile("s_waitcnt vmcnt(0)" ::: "memory");
;         } else {
;             XB_SPIN(xb_ld(&bar[XB_XGEN(b.x)]) == gen, bar);
;             __builtin_amdgcn_fence(__ATOMIC_ACQUIRE, "agent");
;             asm volatile("s_waitcnt vmcnt(0)" ::: "memory");
.LBB0_1216:
	s_or_b64 exec, exec, s[12:13]
	v_cvt_f32_u32_e32 v5, v3
	s_waitcnt vmcnt(0)
	v_readfirstlane_b32 s10, v4
	v_sub_u32_e32 v4, 0, v3
	v_rcp_iflag_f32_e32 v5, v5
	v_add_u32_e32 v6, s10, v2
	v_mul_f32_e32 v5, 0x4f7ffffe, v5
	v_cvt_u32_f32_e32 v5, v5
	v_mul_lo_u32 v2, v4, v5
	v_mul_hi_u32 v2, v5, v2
	v_add_u32_e32 v2, v5, v2
	v_mul_hi_u32 v2, v6, v2
	v_mul_lo_u32 v4, v2, v3
	v_sub_u32_e32 v4, v6, v4
	v_add_u32_e32 v5, 1, v2
	v_cmp_ge_u32_e32 vcc, v4, v3
	s_nop 1
	v_cndmask_b32_e32 v2, v2, v5, vcc
	v_sub_u32_e32 v5, v4, v3
	v_cndmask_b32_e32 v4, v4, v5, vcc
	v_add_u32_e32 v5, 1, v2
	v_cmp_ge_u32_e32 vcc, v4, v3
	v_add_u32_e32 v4, 1, v6
	s_nop 0
	v_cndmask_b32_e32 v2, v2, v5, vcc
	v_mul_lo_u32 v5, v3, v2
	v_add_u32_e32 v3, v5, v3
	v_cmp_ne_u32_e32 vcc, v4, v3
	s_and_saveexec_b64 s[10:11], vcc
	s_xor_b64 s[10:11], exec, s[10:11]
	s_cbranch_execz .LBB0_1230
	s_waitcnt lgkmcnt(0)
	v_mov_b32_e32 v1, 0x2000
	global_load_dword v1, v1, s[8:9] offset:1024 sc1
	s_add_u32 s16, s8, 0x2400
	s_addc_u32 s17, s9, 0
	s_waitcnt vmcnt(0)
	v_cmp_eq_u32_e32 vcc, v1, v2
	buffer_inv sc1
	s_and_saveexec_b64 s[12:13], vcc
	s_cbranch_execz .LBB0_1229
	s_add_u32 s14, s30, 0x4200
	s_addc_u32 s15, s31, 0
	s_mov_b32 s27, 1
	s_mov_b64 s[18:19], 0
	v_mov_b32_e32 v1, 0
	s_branch .LBB0_1220

; __device__ __forceinline__ unsigned xb_ld(unsigned* p)              { return __hip_atomic_load(p, __ATOMIC_RELAXED, __HIP_MEMORY_SCOPE_AGENT); }
; __device__ __forceinline__ unsigned xb_add(unsigned* p, unsigned v) { return __hip_atomic_fetch_add(p, v, __ATOMIC_RELAXED, __HIP_MEMORY_SCOPE_AGENT); }
; #define XB_SPIN(cond, bar) do { unsigned _sp = 0; while (cond) { __builtin_amdgcn_s_sleep(1); \
;     if ((++_sp & 255u) == 0u) { if (xb_ld(&(bar)[XB_TMO])) break; if (_sp > XB_SPIN_CAP) { atomicAdd(&(bar)[XB_TMO], 1u); break; } } } } while (0)
; __device__ __forceinline__ void xcd_barrier(const XcdBarrier& b) {
;     ...
;         const unsigned old = xb_add(&bar[XB_XSUB(b.x)], 1u);
;         const unsigned gen = old / nloc;
;         if (old + 1u == (gen + 1u) * nloc) {
;             __builtin_amdgcn_fence(__ATOMIC_RELEASE, "agent");
;             asm volatile("s_waitcnt vmcnt(0)" ::: "memory");
;             const unsigned og = xb_add(&bar[XB_TOP], 1u);
;             const unsigned tg = og / nx;
;             if (og + 1u == (tg + 1u) * nx) xb_add(&bar[XB_TOPGEN], 1u);
;             else XB_SPIN(xb_ld(&bar[XB_TOPGEN]) == tg, bar);
;             __builtin_amdgcn_fence(__ATOMIC_ACQUIRE, "agent");
;             xb_add(&bar[XB_XGEN(b.x)], 1u);
;             asm volatile("s_waitcnt vmcnt(0)" ::: "memory");
;         } else {
;             XB_SPIN(xb_ld(&bar[XB_XGEN(b.x)]) == gen, bar);
;             __builtin_amdgcn_fence(__ATOMIC_ACQUIRE, "agent");
;             asm volatile("s_waitcnt vmcnt(0)" ::: "memory");
.LBB0_1274:
	s_or_b64 exec, exec, s[12:13]
	v_cvt_f32_u32_e32 v5, v3
	s_waitcnt vmcnt(0)
	v_readfirstlane_b32 s10, v4
	v_sub_u32_e32 v4, 0, v3
	v_rcp_iflag_f32_e32 v5, v5
	v_add_u32_e32 v6, s10, v2
	v_mul_f32_e32 v5, 0x4f7ffffe, v5
	v_cvt_u32_f32_e32 v5, v5
	v_mul_lo_u32 v2, v4, v5
	v_mul_hi_u32 v2, v5, v2
	v_add_u32_e32 v2, v5, v2
	v_mul_hi_u32 v2, v6, v2
	v_mul_lo_u32 v4, v2, v3
	v_sub_u32_e32 v4, v6, v4
	v_add_u32_e32 v5, 1, v2
	v_cmp_ge_u32_e32 vcc, v4, v3
	s_nop 1
	v_cndmask_b32_e32 v2, v2, v5, vcc
	v_sub_u32_e32 v5, v4, v3
	v_cndmask_b32_e32 v4, v4, v5, vcc
	v_add_u32_e32 v5, 1, v2
	v_cmp_ge_u32_e32 vcc, v4, v3
	v_add_u32_e32 v4, 1, v6
	s_nop 0
	v_cndmask_b32_e32 v2, v2, v5, vcc
	v_mul_lo_u32 v5, v3, v2
	v_add_u32_e32 v3, v5, v3
	v_cmp_ne_u32_e32 vcc, v4, v3
	s_and_saveexec_b64 s[10:11], vcc
	s_xor_b64 s[10:11], exec, s[10:11]
	s_cbranch_execz .LBB0_1288
	s_waitcnt lgkmcnt(0)
	v_mov_b32_e32 v1, 0x2000
	global_load_dword v1, v1, s[8:9] offset:1024 sc1
	s_add_u32 s16, s8, 0x2400
	s_addc_u32 s17, s9, 0
	s_waitcnt vmcnt(0)
	v_cmp_eq_u32_e32 vcc, v1, v2
	s_and_saveexec_b64 s[12:13], vcc
	buffer_inv sc1
	s_cbranch_execz .LBB0_1287
	s_add_u32 s14, s30, 0x4200
	s_addc_u32 s15, s31, 0
	s_mov_b32 s27, 1
	s_mov_b64 s[18:19], 0
	v_mov_b32_e32 v1, 0
	s_branch .LBB0_1278

; __device__ __forceinline__ unsigned xb_ld(unsigned* p)              { return __hip_atomic_load(p, __ATOMIC_RELAXED, __HIP_MEMORY_SCOPE_AGENT); }
; __device__ __forceinline__ unsigned xb_add(unsigned* p, unsigned v) { return __hip_atomic_fetch_add(p, v, __ATOMIC_RELAXED, __HIP_MEMORY_SCOPE_AGENT); }
; #define XB_SPIN(cond, bar) do { unsigned _sp = 0; while (cond) { __builtin_amdgcn_s_sleep(1); \
;     if ((++_sp & 255u) == 0u) { if (xb_ld(&(bar)[XB_TMO])) break; if (_sp > XB_SPIN_CAP) { atomicAdd(&(bar)[XB_TMO], 1u); break; } } } } while (0)
; __device__ __forceinline__ void xcd_barrier(const XcdBarrier& b) {
;     ...
;         const unsigned old = xb_add(&bar[XB_XSUB(b.x)], 1u);
;         const unsigned gen = old / nloc;
;         if (old + 1u == (gen + 1u) * nloc) {
;             __builtin_amdgcn_fence(__ATOMIC_RELEASE, "agent");
;             asm volatile("s_waitcnt vmcnt(0)" ::: "memory");
;             const unsigned og = xb_add(&bar[XB_TOP], 1u);
;             const unsigned tg = og / nx;
;             if (og + 1u == (tg + 1u) * nx) xb_add(&bar[XB_TOPGEN], 1u);
;             else XB_SPIN(xb_ld(&bar[XB_TOPGEN]) == tg, bar);
;             __builtin_amdgcn_fence(__ATOMIC_ACQUIRE, "agent");
;             xb_add(&bar[XB_XGEN(b.x)], 1u);
;             asm volatile("s_waitcnt vmcnt(0)" ::: "memory");
;         } else {
;             XB_SPIN(xb_ld(&bar[XB_XGEN(b.x)]) == gen, bar);
;             __builtin_amdgcn_fence(__ATOMIC_ACQUIRE, "agent");
;             asm volatile("s_waitcnt vmcnt(0)" ::: "memory");
.LBB0_1354:
	s_or_b64 exec, exec, s[12:13]
	v_cvt_f32_u32_e32 v5, v3
	s_waitcnt vmcnt(0)
	v_readfirstlane_b32 s10, v4
	v_sub_u32_e32 v4, 0, v3
	v_rcp_iflag_f32_e32 v5, v5
	v_add_u32_e32 v6, s10, v2
	v_mul_f32_e32 v5, 0x4f7ffffe, v5
	v_cvt_u32_f32_e32 v5, v5
	v_mul_lo_u32 v2, v4, v5
	v_mul_hi_u32 v2, v5, v2
	v_add_u32_e32 v2, v5, v2
	v_mul_hi_u32 v2, v6, v2
	v_mul_lo_u32 v4, v2, v3
	v_sub_u32_e32 v4, v6, v4
	v_add_u32_e32 v5, 1, v2
	v_cmp_ge_u32_e32 vcc, v4, v3
	s_nop 1
	v_cndmask_b32_e32 v2, v2, v5, vcc
	v_sub_u32_e32 v5, v4, v3
	v_cndmask_b32_e32 v4, v4, v5, vcc
	v_add_u32_e32 v5, 1, v2
	v_cmp_ge_u32_e32 vcc, v4, v3
	v_add_u32_e32 v4, 1, v6
	s_nop 0
	v_cndmask_b32_e32 v2, v2, v5, vcc
	v_mul_lo_u32 v5, v3, v2
	v_add_u32_e32 v3, v5, v3
	v_cmp_ne_u32_e32 vcc, v4, v3
	s_and_saveexec_b64 s[10:11], vcc
	s_xor_b64 s[10:11], exec, s[10:11]
	s_cbranch_execz .LBB0_1368
	s_waitcnt lgkmcnt(0)
	v_mov_b32_e32 v1, 0x2000
	global_load_dword v1, v1, s[8:9] offset:1024 sc1
	s_add_u32 s16, s8, 0x2400
	s_addc_u32 s17, s9, 0
	s_waitcnt vmcnt(0)
	v_cmp_eq_u32_e32 vcc, v1, v2
	s_and_saveexec_b64 s[12:13], vcc
	s_cbranch_execz .LBB0_1367
	buffer_inv sc1
	s_add_u32 s14, s30, 0x4200
	s_addc_u32 s15, s31, 0
	s_mov_b32 s27, 1
	s_mov_b64 s[18:19], 0
	v_mov_b32_e32 v1, 0
	s_branch .LBB0_1358

; __device__ __forceinline__ unsigned xb_ld(unsigned* p)              { return __hip_atomic_load(p, __ATOMIC_RELAXED, __HIP_MEMORY_SCOPE_AGENT); }
; __device__ __forceinline__ unsigned xb_add(unsigned* p, unsigned v) { return __hip_atomic_fetch_add(p, v, __ATOMIC_RELAXED, __HIP_MEMORY_SCOPE_AGENT); }
; #define XB_SPIN(cond, bar) do { unsigned _sp = 0; while (cond) { __builtin_amdgcn_s_sleep(1); \
;     if ((++_sp & 255u) == 0u) { if (xb_ld(&(bar)[XB_TMO])) break; if (_sp > XB_SPIN_CAP) { atomicAdd(&(bar)[XB_TMO], 1u); break; } } } } while (0)
; __device__ __forceinline__ void xcd_barrier(const XcdBarrier& b) {
;     ...
;         const unsigned old = xb_add(&bar[XB_XSUB(b.x)], 1u);
;         const unsigned gen = old / nloc;
;         if (old + 1u == (gen + 1u) * nloc) {
;             __builtin_amdgcn_fence(__ATOMIC_RELEASE, "agent");
;             asm volatile("s_waitcnt vmcnt(0)" ::: "memory");
;             const unsigned og = xb_add(&bar[XB_TOP], 1u);
;             const unsigned tg = og / nx;
;             if (og + 1u == (tg + 1u) * nx) xb_add(&bar[XB_TOPGEN], 1u);
;             else XB_SPIN(xb_ld(&bar[XB_TOPGEN]) == tg, bar);
;             __builtin_amdgcn_fence(__ATOMIC_ACQUIRE, "agent");
;             xb_add(&bar[XB_XGEN(b.x)], 1u);
;             asm volatile("s_waitcnt vmcnt(0)" ::: "memory");
;         } else {
;             XB_SPIN(xb_ld(&bar[XB_XGEN(b.x)]) == gen, bar);
;             __builtin_amdgcn_fence(__ATOMIC_ACQUIRE, "agent");
;             asm volatile("s_waitcnt vmcnt(0)" ::: "memory");
.LBB0_1516:
	s_or_b64 exec, exec, s[12:13]
	v_cvt_f32_u32_e32 v5, v3
	s_waitcnt vmcnt(0)
	v_readfirstlane_b32 s10, v4
	v_sub_u32_e32 v4, 0, v3
	v_rcp_iflag_f32_e32 v5, v5
	v_add_u32_e32 v6, s10, v2
	v_mul_f32_e32 v5, 0x4f7ffffe, v5
	v_cvt_u32_f32_e32 v5, v5
	v_mul_lo_u32 v2, v4, v5
	v_mul_hi_u32 v2, v5, v2
	v_add_u32_e32 v2, v5, v2
	v_mul_hi_u32 v2, v6, v2
	v_mul_lo_u32 v4, v2, v3
	v_sub_u32_e32 v4, v6, v4
	v_add_u32_e32 v5, 1, v2
	v_cmp_ge_u32_e32 vcc, v4, v3
	s_nop 1
	v_cndmask_b32_e32 v2, v2, v5, vcc
	v_sub_u32_e32 v5, v4, v3
	v_cndmask_b32_e32 v4, v4, v5, vcc
	v_add_u32_e32 v5, 1, v2
	v_cmp_ge_u32_e32 vcc, v4, v3
	v_add_u32_e32 v4, 1, v6
	s_nop 0
	v_cndmask_b32_e32 v2, v2, v5, vcc
	v_mul_lo_u32 v5, v3, v2
	v_add_u32_e32 v3, v5, v3
	v_cmp_ne_u32_e32 vcc, v4, v3
	s_and_saveexec_b64 s[10:11], vcc
	s_xor_b64 s[10:11], exec, s[10:11]
	s_cbranch_execz .LBB0_1530
	s_waitcnt lgkmcnt(0)
	v_mov_b32_e32 v1, 0x2000
	global_load_dword v1, v1, s[8:9] offset:1024 sc1
	s_add_u32 s16, s8, 0x2400
	s_addc_u32 s17, s9, 0
	s_waitcnt vmcnt(0)
	v_cmp_eq_u32_e32 vcc, v1, v2
	s_and_saveexec_b64 s[12:13], vcc
	s_cbranch_execz .LBB0_1529
	s_add_u32 s14, s30, 0x4200
	buffer_inv sc1
	s_addc_u32 s15, s31, 0
	s_mov_b32 s27, 1
	s_mov_b64 s[18:19], 0
	v_mov_b32_e32 v1, 0
	s_branch .LBB0_1520

; __device__ __forceinline__ unsigned xb_ld(unsigned* p)              { return __hip_atomic_load(p, __ATOMIC_RELAXED, __HIP_MEMORY_SCOPE_AGENT); }
; __device__ __forceinline__ unsigned xb_add(unsigned* p, unsigned v) { return __hip_atomic_fetch_add(p, v, __ATOMIC_RELAXED, __HIP_MEMORY_SCOPE_AGENT); }
; #define XB_SPIN(cond, bar) do { unsigned _sp = 0; while (cond) { __builtin_amdgcn_s_sleep(1); \
;     if ((++_sp & 255u) == 0u) { if (xb_ld(&(bar)[XB_TMO])) break; if (_sp > XB_SPIN_CAP) { atomicAdd(&(bar)[XB_TMO], 1u); break; } } } } while (0)
; __device__ __forceinline__ void xcd_barrier(const XcdBarrier& b) {
;     ...
;         const unsigned old = xb_add(&bar[XB_XSUB(b.x)], 1u);
;         const unsigned gen = old / nloc;
;         if (old + 1u == (gen + 1u) * nloc) {
;             __builtin_amdgcn_fence(__ATOMIC_RELEASE, "agent");
;             asm volatile("s_waitcnt vmcnt(0)" ::: "memory");
;             const unsigned og = xb_add(&bar[XB_TOP], 1u);
;             const unsigned tg = og / nx;
;             if (og + 1u == (tg + 1u) * nx) xb_add(&bar[XB_TOPGEN], 1u);
;             else XB_SPIN(xb_ld(&bar[XB_TOPGEN]) == tg, bar);
;             __builtin_amdgcn_fence(__ATOMIC_ACQUIRE, "agent");
;             xb_add(&bar[XB_XGEN(b.x)], 1u);
;             asm volatile("s_waitcnt vmcnt(0)" ::: "memory");
;         } else {
;             XB_SPIN(xb_ld(&bar[XB_XGEN(b.x)]) == gen, bar);
;             __builtin_amdgcn_fence(__ATOMIC_ACQUIRE, "agent");
;             asm volatile("s_waitcnt vmcnt(0)" ::: "memory");
.LBB0_1648:
	s_or_b64 exec, exec, s[14:15]
	v_cvt_f32_u32_e32 v5, v3
	s_waitcnt vmcnt(0)
	v_readfirstlane_b32 s12, v4
	v_sub_u32_e32 v4, 0, v3
	v_rcp_iflag_f32_e32 v5, v5
	v_add_u32_e32 v6, s12, v2
	v_mul_f32_e32 v5, 0x4f7ffffe, v5
	v_cvt_u32_f32_e32 v5, v5
	v_mul_lo_u32 v2, v4, v5
	v_mul_hi_u32 v2, v5, v2
	v_add_u32_e32 v2, v5, v2
	v_mul_hi_u32 v2, v6, v2
	v_mul_lo_u32 v4, v2, v3
	v_sub_u32_e32 v4, v6, v4
	v_add_u32_e32 v5, 1, v2
	v_cmp_ge_u32_e32 vcc, v4, v3
	s_nop 1
	v_cndmask_b32_e32 v2, v2, v5, vcc
	v_sub_u32_e32 v5, v4, v3
	v_cndmask_b32_e32 v4, v4, v5, vcc
	v_add_u32_e32 v5, 1, v2
	v_cmp_ge_u32_e32 vcc, v4, v3
	v_add_u32_e32 v4, 1, v6
	s_nop 0
	v_cndmask_b32_e32 v2, v2, v5, vcc
	v_mul_lo_u32 v5, v3, v2
	v_add_u32_e32 v3, v5, v3
	v_cmp_ne_u32_e32 vcc, v4, v3
	s_and_saveexec_b64 s[12:13], vcc
	s_xor_b64 s[12:13], exec, s[12:13]
	s_cbranch_execz .LBB0_1662
	s_waitcnt lgkmcnt(0)
	v_mov_b32_e32 v1, 0x2000
	global_load_dword v1, v1, s[10:11] offset:1024 sc1
	s_add_u32 s18, s10, 0x2400
	s_addc_u32 s19, s11, 0
	s_waitcnt vmcnt(0)
	v_cmp_eq_u32_e32 vcc, v1, v2
	s_and_saveexec_b64 s[14:15], vcc
	s_cbranch_execz .LBB0_1661
	s_add_u32 s16, s30, 0x4200
	s_addc_u32 s17, s31, 0
	buffer_inv sc1
	s_mov_b32 s36, 1
	s_mov_b64 s[22:23], 0
	v_mov_b32_e32 v1, 0
	s_branch .LBB0_1652

; __device__ __forceinline__ unsigned xb_ld(unsigned* p)              { return __hip_atomic_load(p, __ATOMIC_RELAXED, __HIP_MEMORY_SCOPE_AGENT); }
; #define XB_SPIN(cond, bar) do { unsigned _sp = 0; while (cond) { __builtin_amdgcn_s_sleep(1); \
;     if ((++_sp & 255u) == 0u) { if (xb_ld(&(bar)[XB_TMO])) break; if (_sp > XB_SPIN_CAP) { atomicAdd(&(bar)[XB_TMO], 1u); break; } } } } while (0)
; __device__ __forceinline__ void xcd_barrier(const XcdBarrier& b) {
;     ...
;         } else {
;             XB_SPIN(xb_ld(&bar[XB_XGEN(b.x)]) == gen, bar);
;             __builtin_amdgcn_fence(__ATOMIC_ACQUIRE, "agent");
;             asm volatile("s_waitcnt vmcnt(0)" ::: "memory");
;         }
.LBB0_1661:
	s_or_b64 exec, exec, s[14:15]
	s_waitcnt vmcnt(0)
	s_waitcnt vmcnt(0)

; __device__ __forceinline__ unsigned xb_ld(unsigned* p)              { return __hip_atomic_load(p, __ATOMIC_RELAXED, __HIP_MEMORY_SCOPE_AGENT); }
; __device__ __forceinline__ unsigned xb_add(unsigned* p, unsigned v) { return __hip_atomic_fetch_add(p, v, __ATOMIC_RELAXED, __HIP_MEMORY_SCOPE_AGENT); }
; #define XB_SPIN(cond, bar) do { unsigned _sp = 0; while (cond) { __builtin_amdgcn_s_sleep(1); \
;     if ((++_sp & 255u) == 0u) { if (xb_ld(&(bar)[XB_TMO])) break; if (_sp > XB_SPIN_CAP) { atomicAdd(&(bar)[XB_TMO], 1u); break; } } } } while (0)
; __device__ __forceinline__ void xcd_barrier(const XcdBarrier& b) {
;     ...
;         const unsigned old = xb_add(&bar[XB_XSUB(b.x)], 1u);
;         const unsigned gen = old / nloc;
;         if (old + 1u == (gen + 1u) * nloc) {
;             __builtin_amdgcn_fence(__ATOMIC_RELEASE, "agent");
;             asm volatile("s_waitcnt vmcnt(0)" ::: "memory");
;             const unsigned og = xb_add(&bar[XB_TOP], 1u);
;             const unsigned tg = og / nx;
;             if (og + 1u == (tg + 1u) * nx) xb_add(&bar[XB_TOPGEN], 1u);
;             else XB_SPIN(xb_ld(&bar[XB_TOPGEN]) == tg, bar);
;             __builtin_amdgcn_fence(__ATOMIC_ACQUIRE, "agent");
;             xb_add(&bar[XB_XGEN(b.x)], 1u);
;             asm volatile("s_waitcnt vmcnt(0)" ::: "memory");
;         } else {
;             XB_SPIN(xb_ld(&bar[XB_XGEN(b.x)]) == gen, bar);
;             __builtin_amdgcn_fence(__ATOMIC_ACQUIRE, "agent");
;             asm volatile("s_waitcnt vmcnt(0)" ::: "memory");
.LBB0_1727:
	s_or_b64 exec, exec, s[12:13]
	v_cvt_f32_u32_e32 v5, v3
	s_waitcnt vmcnt(0)
	v_readfirstlane_b32 s3, v4
	v_sub_u32_e32 v4, 0, v3
	v_rcp_iflag_f32_e32 v5, v5
	v_add_u32_e32 v6, s3, v2
	v_mul_f32_e32 v5, 0x4f7ffffe, v5
	v_cvt_u32_f32_e32 v5, v5
	v_mul_lo_u32 v2, v4, v5
	v_mul_hi_u32 v2, v5, v2
	v_add_u32_e32 v2, v5, v2
	v_mul_hi_u32 v2, v6, v2
	v_mul_lo_u32 v4, v2, v3
	v_sub_u32_e32 v4, v6, v4
	v_add_u32_e32 v5, 1, v2
	v_cmp_ge_u32_e32 vcc, v4, v3
	s_nop 1
	v_cndmask_b32_e32 v2, v2, v5, vcc
	v_sub_u32_e32 v5, v4, v3
	v_cndmask_b32_e32 v4, v4, v5, vcc
	v_add_u32_e32 v5, 1, v2
	v_cmp_ge_u32_e32 vcc, v4, v3
	v_add_u32_e32 v4, 1, v6
	s_nop 0
	v_cndmask_b32_e32 v2, v2, v5, vcc
	v_mul_lo_u32 v5, v3, v2
	v_add_u32_e32 v3, v5, v3
	v_cmp_ne_u32_e32 vcc, v4, v3
	s_and_saveexec_b64 s[10:11], vcc
	s_xor_b64 s[10:11], exec, s[10:11]
	s_cbranch_execz .LBB0_1741
	s_waitcnt lgkmcnt(0)
	v_mov_b32_e32 v1, 0x2000
	global_load_dword v1, v1, s[8:9] offset:1024 sc1
	s_add_u32 s16, s8, 0x2400
	s_addc_u32 s17, s9, 0
	s_waitcnt vmcnt(0)
	v_cmp_eq_u32_e32 vcc, v1, v2
	s_and_saveexec_b64 s[12:13], vcc
	s_cbranch_execz .LBB0_1740
	s_add_u32 s14, s30, 0x4200
	s_addc_u32 s15, s31, 0
	s_mov_b32 s3, 1
	buffer_inv sc1
	s_mov_b64 s[18:19], 0
	v_mov_b32_e32 v1, 0
	s_branch .LBB0_1731
